# T9 grid barrier release flattened: non-leader workgroups poll the cross-XCD generation word directly, leader's per-XCD bump and its waits removed (on top of v10)
# speedup vs baseline: 1.0025x; 1.0025x over previous
; __device__ __forceinline__ unsigned xb_ld(unsigned* p)              { return __hip_atomic_load(p, __ATOMIC_RELAXED, __HIP_MEMORY_SCOPE_AGENT); }
; __device__ __forceinline__ unsigned xb_add(unsigned* p, unsigned v) { return __hip_atomic_fetch_add(p, v, __ATOMIC_RELAXED, __HIP_MEMORY_SCOPE_AGENT); }
; #define XB_SPIN(cond, bar) do { unsigned _sp = 0; while (cond) { __builtin_amdgcn_s_sleep(1); \
;     if ((++_sp & 255u) == 0u) { if (xb_ld(&(bar)[XB_TMO])) break; if (_sp > XB_SPIN_CAP) { atomicAdd(&(bar)[XB_TMO], 1u); break; } } } } while (0)
; __device__ __forceinline__ void xcd_barrier(const XcdBarrier& b) {
;     ...
;     if (threadIdx.x == 0) {
;         unsigned* bar = b.bar;
;         __builtin_amdgcn_s_waitcnt(0);
;         unsigned nloc = b.st[0], nx = b.st[1];
;         if (nloc == 0u) { xcd_barrier_complete(bar, b.x, nloc, nx); b.st[0] = nloc; b.st[1] = nx; }
;         const unsigned old = xb_add(&bar[XB_XSUB(b.x)], 1u);
;         const unsigned gen = old / nloc;
;         if (old + 1u == (gen + 1u) * nloc) {
;             __builtin_amdgcn_fence(__ATOMIC_RELEASE, "agent");
;             asm volatile("s_waitcnt vmcnt(0)" ::: "memory");
;             const unsigned og = xb_add(&bar[XB_TOP], 1u);
;             const unsigned tg = og / nx;
;             if (og + 1u == (tg + 1u) * nx) xb_add(&bar[XB_TOPGEN], 1u);
;             else XB_SPIN(xb_ld(&bar[XB_TOPGEN]) == tg, bar);
;             __builtin_amdgcn_fence(__ATOMIC_ACQUIRE, "agent");
;             xb_add(&bar[XB_XGEN(b.x)], 1u);
;             asm volatile("s_waitcnt vmcnt(0)" ::: "memory");
;         } else {
;             XB_SPIN(xb_ld(&bar[XB_XGEN(b.x)]) == gen, bar);
.LBB0_266:
	v_readlane_b32 s4, v247, 7
	s_lshl_b32 s4, s4, 8
	s_add_u32 s4, s72, s4
	s_addc_u32 s5, s73, 0
	v_mov_b32_e32 v2, 0x1000
	v_mov_b32_e32 v4, 1
	global_atomic_add v4, v2, v4, s[4:5] offset:1024 sc0
	buffer_inv sc1
	v_cvt_f32_u32_e32 v2, v3
	v_sub_u32_e32 v5, 0, v3
	v_rcp_iflag_f32_e32 v2, v2
	s_nop 0
	v_mul_f32_e32 v2, 0x4f7ffffe, v2
	v_cvt_u32_f32_e32 v2, v2
	v_mul_lo_u32 v5, v5, v2
	v_mul_hi_u32 v5, v2, v5
	v_add_u32_e32 v2, v2, v5
	s_waitcnt vmcnt(1)
	v_mul_hi_u32 v2, v4, v2
	v_mul_lo_u32 v5, v2, v3
	v_sub_u32_e32 v5, v4, v5
	v_add_u32_e32 v6, 1, v2
	v_cmp_ge_u32_e32 vcc, v5, v3
	v_add_u32_e32 v4, 1, v4
	s_nop 0
	v_cndmask_b32_e32 v2, v2, v6, vcc
	v_sub_u32_e32 v6, v5, v3
	v_cndmask_b32_e32 v5, v5, v6, vcc
	v_add_u32_e32 v6, 1, v2
	v_cmp_ge_u32_e32 vcc, v5, v3
	s_nop 1
	v_cndmask_b32_e32 v2, v2, v6, vcc
	v_mul_lo_u32 v5, v3, v2
	v_add_u32_e32 v3, v5, v3
	v_cmp_ne_u32_e32 vcc, v4, v3
	s_and_saveexec_b64 s[6:7], vcc
	s_xor_b64 s[6:7], exec, s[6:7]
	s_cbranch_execz .LBB0_280
	s_waitcnt lgkmcnt(0)
	v_mov_b32_e32 v1, 0x7100
	global_load_dword v1, v1, s[86:87] offset:1024 sc1
	s_add_u32 s12, s86, 0x7500
	s_addc_u32 s13, s87, 0
	s_waitcnt vmcnt(0)
	v_cmp_eq_u32_e32 vcc, v1, v2
	s_and_saveexec_b64 s[8:9], vcc
	s_cbranch_execz .LBB0_279
	s_add_u32 s10, s86, 0x4200
	s_addc_u32 s11, s87, 0
	s_mov_b32 s24, 1
	s_mov_b64 s[14:15], 0
	v_mov_b32_e32 v1, 0
	s_branch .LBB0_270

; __device__ __forceinline__ unsigned xb_ld(unsigned* p)              { return __hip_atomic_load(p, __ATOMIC_RELAXED, __HIP_MEMORY_SCOPE_AGENT); }
; __device__ __forceinline__ unsigned xb_add(unsigned* p, unsigned v) { return __hip_atomic_fetch_add(p, v, __ATOMIC_RELAXED, __HIP_MEMORY_SCOPE_AGENT); }
; #define XB_SPIN(cond, bar) do { unsigned _sp = 0; while (cond) { __builtin_amdgcn_s_sleep(1); \
;     if ((++_sp & 255u) == 0u) { if (xb_ld(&(bar)[XB_TMO])) break; if (_sp > XB_SPIN_CAP) { atomicAdd(&(bar)[XB_TMO], 1u); break; } } } } while (0)
; __device__ __forceinline__ void xcd_barrier(const XcdBarrier& b) {
;     ...
;         if (old + 1u == (gen + 1u) * nloc) {
;             __builtin_amdgcn_fence(__ATOMIC_RELEASE, "agent");
;             asm volatile("s_waitcnt vmcnt(0)" ::: "memory");
;             const unsigned og = xb_add(&bar[XB_TOP], 1u);
;             const unsigned tg = og / nx;
;             if (og + 1u == (tg + 1u) * nx) xb_add(&bar[XB_TOPGEN], 1u);
;             else XB_SPIN(xb_ld(&bar[XB_TOPGEN]) == tg, bar);
;             __builtin_amdgcn_fence(__ATOMIC_ACQUIRE, "agent");
;             xb_add(&bar[XB_XGEN(b.x)], 1u);
;             asm volatile("s_waitcnt vmcnt(0)" ::: "memory");
.LBB0_297:
	s_or_b64 exec, exec, s[6:7]
.LBB0_298:
	s_or_b64 exec, exec, s[0:1]
	s_waitcnt lgkmcnt(0)
	s_barrier

; __device__ __forceinline__ unsigned xb_ld(unsigned* p)              { return __hip_atomic_load(p, __ATOMIC_RELAXED, __HIP_MEMORY_SCOPE_AGENT); }
; __device__ __forceinline__ unsigned xb_add(unsigned* p, unsigned v) { return __hip_atomic_fetch_add(p, v, __ATOMIC_RELAXED, __HIP_MEMORY_SCOPE_AGENT); }
; #define XB_SPIN(cond, bar) do { unsigned _sp = 0; while (cond) { __builtin_amdgcn_s_sleep(1); \
;     if ((++_sp & 255u) == 0u) { if (xb_ld(&(bar)[XB_TMO])) break; if (_sp > XB_SPIN_CAP) { atomicAdd(&(bar)[XB_TMO], 1u); break; } } } } while (0)
; __device__ __forceinline__ void xcd_barrier(const XcdBarrier& b) {
;     ...
;         if (old + 1u == (gen + 1u) * nloc) {
;             __builtin_amdgcn_fence(__ATOMIC_RELEASE, "agent");
;             asm volatile("s_waitcnt vmcnt(0)" ::: "memory");
;             const unsigned og = xb_add(&bar[XB_TOP], 1u);
;             const unsigned tg = og / nx;
;             if (og + 1u == (tg + 1u) * nx) xb_add(&bar[XB_TOPGEN], 1u);
;             else XB_SPIN(xb_ld(&bar[XB_TOPGEN]) == tg, bar);
;             __builtin_amdgcn_fence(__ATOMIC_ACQUIRE, "agent");
;             xb_add(&bar[XB_XGEN(b.x)], 1u);
;             asm volatile("s_waitcnt vmcnt(0)" ::: "memory");
.LBB0_355:
	s_or_b64 exec, exec, s[6:7]
.LBB0_356:
	s_or_b64 exec, exec, s[0:1]
	s_waitcnt lgkmcnt(0)
	s_barrier

; __device__ __forceinline__ unsigned xb_ld(unsigned* p)              { return __hip_atomic_load(p, __ATOMIC_RELAXED, __HIP_MEMORY_SCOPE_AGENT); }
; __device__ __forceinline__ unsigned xb_add(unsigned* p, unsigned v) { return __hip_atomic_fetch_add(p, v, __ATOMIC_RELAXED, __HIP_MEMORY_SCOPE_AGENT); }
; #define XB_SPIN(cond, bar) do { unsigned _sp = 0; while (cond) { __builtin_amdgcn_s_sleep(1); \
;     if ((++_sp & 255u) == 0u) { if (xb_ld(&(bar)[XB_TMO])) break; if (_sp > XB_SPIN_CAP) { atomicAdd(&(bar)[XB_TMO], 1u); break; } } } } while (0)
; __device__ __forceinline__ void xcd_barrier(const XcdBarrier& b) {
;     ...
;         if (old + 1u == (gen + 1u) * nloc) {
;             __builtin_amdgcn_fence(__ATOMIC_RELEASE, "agent");
;             asm volatile("s_waitcnt vmcnt(0)" ::: "memory");
;             const unsigned og = xb_add(&bar[XB_TOP], 1u);
;             const unsigned tg = og / nx;
;             if (og + 1u == (tg + 1u) * nx) xb_add(&bar[XB_TOPGEN], 1u);
;             else XB_SPIN(xb_ld(&bar[XB_TOPGEN]) == tg, bar);
;             __builtin_amdgcn_fence(__ATOMIC_ACQUIRE, "agent");
;             xb_add(&bar[XB_XGEN(b.x)], 1u);
;             asm volatile("s_waitcnt vmcnt(0)" ::: "memory");
.LBB0_454:
	s_or_b64 exec, exec, s[6:7]
.LBB0_455:
	s_or_b64 exec, exec, s[0:1]
	s_waitcnt lgkmcnt(0)
	s_barrier

; __device__ __forceinline__ unsigned xb_ld(unsigned* p)              { return __hip_atomic_load(p, __ATOMIC_RELAXED, __HIP_MEMORY_SCOPE_AGENT); }
; __device__ __forceinline__ unsigned xb_add(unsigned* p, unsigned v) { return __hip_atomic_fetch_add(p, v, __ATOMIC_RELAXED, __HIP_MEMORY_SCOPE_AGENT); }
; #define XB_SPIN(cond, bar) do { unsigned _sp = 0; while (cond) { __builtin_amdgcn_s_sleep(1); \
;     if ((++_sp & 255u) == 0u) { if (xb_ld(&(bar)[XB_TMO])) break; if (_sp > XB_SPIN_CAP) { atomicAdd(&(bar)[XB_TMO], 1u); break; } } } } while (0)
; __device__ __forceinline__ void xcd_barrier(const XcdBarrier& b) {
;     ...
;         if (old + 1u == (gen + 1u) * nloc) {
;             __builtin_amdgcn_fence(__ATOMIC_RELEASE, "agent");
;             asm volatile("s_waitcnt vmcnt(0)" ::: "memory");
;             const unsigned og = xb_add(&bar[XB_TOP], 1u);
;             const unsigned tg = og / nx;
;             if (og + 1u == (tg + 1u) * nx) xb_add(&bar[XB_TOPGEN], 1u);
;             else XB_SPIN(xb_ld(&bar[XB_TOPGEN]) == tg, bar);
;             __builtin_amdgcn_fence(__ATOMIC_ACQUIRE, "agent");
;             xb_add(&bar[XB_XGEN(b.x)], 1u);
;             asm volatile("s_waitcnt vmcnt(0)" ::: "memory");
.LBB0_574:
	s_or_b64 exec, exec, s[6:7]
.LBB0_575:
	s_or_b64 exec, exec, s[2:3]
	s_waitcnt lgkmcnt(0)
	s_barrier

; __device__ __forceinline__ unsigned xb_ld(unsigned* p)              { return __hip_atomic_load(p, __ATOMIC_RELAXED, __HIP_MEMORY_SCOPE_AGENT); }
; __device__ __forceinline__ unsigned xb_add(unsigned* p, unsigned v) { return __hip_atomic_fetch_add(p, v, __ATOMIC_RELAXED, __HIP_MEMORY_SCOPE_AGENT); }
; #define XB_SPIN(cond, bar) do { unsigned _sp = 0; while (cond) { __builtin_amdgcn_s_sleep(1); \
;     if ((++_sp & 255u) == 0u) { if (xb_ld(&(bar)[XB_TMO])) break; if (_sp > XB_SPIN_CAP) { atomicAdd(&(bar)[XB_TMO], 1u); break; } } } } while (0)
; __device__ __forceinline__ void xcd_barrier(const XcdBarrier& b) {
;     ...
;     if (threadIdx.x == 0) {
;         unsigned* bar = b.bar;
;         __builtin_amdgcn_s_waitcnt(0);
;         unsigned nloc = b.st[0], nx = b.st[1];
;         if (nloc == 0u) { xcd_barrier_complete(bar, b.x, nloc, nx); b.st[0] = nloc; b.st[1] = nx; }
;         const unsigned old = xb_add(&bar[XB_XSUB(b.x)], 1u);
;         const unsigned gen = old / nloc;
;         if (old + 1u == (gen + 1u) * nloc) {
;             __builtin_amdgcn_fence(__ATOMIC_RELEASE, "agent");
;             asm volatile("s_waitcnt vmcnt(0)" ::: "memory");
;             const unsigned og = xb_add(&bar[XB_TOP], 1u);
;             const unsigned tg = og / nx;
;             if (og + 1u == (tg + 1u) * nx) xb_add(&bar[XB_TOPGEN], 1u);
;             else XB_SPIN(xb_ld(&bar[XB_TOPGEN]) == tg, bar);
;             __builtin_amdgcn_fence(__ATOMIC_ACQUIRE, "agent");
;             xb_add(&bar[XB_XGEN(b.x)], 1u);
;             asm volatile("s_waitcnt vmcnt(0)" ::: "memory");
;         } else {
;             XB_SPIN(xb_ld(&bar[XB_XGEN(b.x)]) == gen, bar);
.LBB0_696:
	v_readlane_b32 s4, v247, 7
	s_lshl_b32 s4, s4, 8
	s_add_u32 s4, s72, s4
	s_addc_u32 s5, s73, 0
	v_mov_b32_e32 v3, 0x1000
	v_mov_b32_e32 v5, 1
	global_atomic_add v5, v3, v5, s[4:5] offset:1024 sc0
	buffer_inv sc1
	v_cvt_f32_u32_e32 v3, v4
	v_sub_u32_e32 v6, 0, v4
	v_rcp_iflag_f32_e32 v3, v3
	s_nop 0
	v_mul_f32_e32 v3, 0x4f7ffffe, v3
	v_cvt_u32_f32_e32 v3, v3
	v_mul_lo_u32 v6, v6, v3
	v_mul_hi_u32 v6, v3, v6
	v_add_u32_e32 v3, v3, v6
	s_waitcnt vmcnt(1)
	v_mul_hi_u32 v3, v5, v3
	v_mul_lo_u32 v6, v3, v4
	v_sub_u32_e32 v6, v5, v6
	v_add_u32_e32 v7, 1, v3
	v_cmp_ge_u32_e32 vcc, v6, v4
	v_add_u32_e32 v5, 1, v5
	s_nop 0
	v_cndmask_b32_e32 v3, v3, v7, vcc
	v_sub_u32_e32 v7, v6, v4
	v_cndmask_b32_e32 v6, v6, v7, vcc
	v_add_u32_e32 v7, 1, v3
	v_cmp_ge_u32_e32 vcc, v6, v4
	s_nop 1
	v_cndmask_b32_e32 v3, v3, v7, vcc
	v_mul_lo_u32 v6, v4, v3
	v_add_u32_e32 v4, v6, v4
	v_cmp_ne_u32_e32 vcc, v5, v4
	s_and_saveexec_b64 s[6:7], vcc
	s_xor_b64 s[6:7], exec, s[6:7]
	s_cbranch_execz .LBB0_710
	s_waitcnt lgkmcnt(0)
	v_mov_b32_e32 v2, 0x7100
	global_load_dword v2, v2, s[86:87] offset:1024 sc1
	s_add_u32 s12, s86, 0x7500
	s_addc_u32 s13, s87, 0
	s_waitcnt vmcnt(0)
	v_cmp_eq_u32_e32 vcc, v2, v3
	s_and_saveexec_b64 s[8:9], vcc
	s_cbranch_execz .LBB0_709
	s_add_u32 s10, s86, 0x4200
	s_addc_u32 s11, s87, 0
	s_mov_b32 s24, 1
	s_mov_b64 s[14:15], 0
	v_mov_b32_e32 v2, 0
	s_branch .LBB0_700

; __device__ __forceinline__ unsigned xb_ld(unsigned* p)              { return __hip_atomic_load(p, __ATOMIC_RELAXED, __HIP_MEMORY_SCOPE_AGENT); }
; __device__ __forceinline__ unsigned xb_add(unsigned* p, unsigned v) { return __hip_atomic_fetch_add(p, v, __ATOMIC_RELAXED, __HIP_MEMORY_SCOPE_AGENT); }
; #define XB_SPIN(cond, bar) do { unsigned _sp = 0; while (cond) { __builtin_amdgcn_s_sleep(1); \
;     if ((++_sp & 255u) == 0u) { if (xb_ld(&(bar)[XB_TMO])) break; if (_sp > XB_SPIN_CAP) { atomicAdd(&(bar)[XB_TMO], 1u); break; } } } } while (0)
; __device__ __forceinline__ void xcd_barrier(const XcdBarrier& b) {
;     ...
;         if (old + 1u == (gen + 1u) * nloc) {
;             __builtin_amdgcn_fence(__ATOMIC_RELEASE, "agent");
;             asm volatile("s_waitcnt vmcnt(0)" ::: "memory");
;             const unsigned og = xb_add(&bar[XB_TOP], 1u);
;             const unsigned tg = og / nx;
;             if (og + 1u == (tg + 1u) * nx) xb_add(&bar[XB_TOPGEN], 1u);
;             else XB_SPIN(xb_ld(&bar[XB_TOPGEN]) == tg, bar);
;             __builtin_amdgcn_fence(__ATOMIC_ACQUIRE, "agent");
;             xb_add(&bar[XB_XGEN(b.x)], 1u);
;             asm volatile("s_waitcnt vmcnt(0)" ::: "memory");
.LBB0_727:
	s_or_b64 exec, exec, s[6:7]
.LBB0_728:
	s_or_b64 exec, exec, s[2:3]
	s_waitcnt lgkmcnt(0)
	s_barrier

; __device__ __forceinline__ unsigned xb_ld(unsigned* p)              { return __hip_atomic_load(p, __ATOMIC_RELAXED, __HIP_MEMORY_SCOPE_AGENT); }
; __device__ __forceinline__ unsigned xb_add(unsigned* p, unsigned v) { return __hip_atomic_fetch_add(p, v, __ATOMIC_RELAXED, __HIP_MEMORY_SCOPE_AGENT); }
; #define XB_SPIN(cond, bar) do { unsigned _sp = 0; while (cond) { __builtin_amdgcn_s_sleep(1); \
;     if ((++_sp & 255u) == 0u) { if (xb_ld(&(bar)[XB_TMO])) break; if (_sp > XB_SPIN_CAP) { atomicAdd(&(bar)[XB_TMO], 1u); break; } } } } while (0)
; __device__ __forceinline__ void xcd_barrier(const XcdBarrier& b) {
;     ...
;         if (old + 1u == (gen + 1u) * nloc) {
;             __builtin_amdgcn_fence(__ATOMIC_RELEASE, "agent");
;             asm volatile("s_waitcnt vmcnt(0)" ::: "memory");
;             const unsigned og = xb_add(&bar[XB_TOP], 1u);
;             const unsigned tg = og / nx;
;             if (og + 1u == (tg + 1u) * nx) xb_add(&bar[XB_TOPGEN], 1u);
;             else XB_SPIN(xb_ld(&bar[XB_TOPGEN]) == tg, bar);
;             __builtin_amdgcn_fence(__ATOMIC_ACQUIRE, "agent");
;             xb_add(&bar[XB_XGEN(b.x)], 1u);
;             asm volatile("s_waitcnt vmcnt(0)" ::: "memory");
.LBB0_802:
	s_or_b64 exec, exec, s[6:7]
.LBB0_803:
	s_or_b64 exec, exec, s[0:1]
	s_waitcnt lgkmcnt(0)
	s_barrier

; __device__ __forceinline__ unsigned xb_ld(unsigned* p)              { return __hip_atomic_load(p, __ATOMIC_RELAXED, __HIP_MEMORY_SCOPE_AGENT); }
; __device__ __forceinline__ unsigned xb_add(unsigned* p, unsigned v) { return __hip_atomic_fetch_add(p, v, __ATOMIC_RELAXED, __HIP_MEMORY_SCOPE_AGENT); }
; #define XB_SPIN(cond, bar) do { unsigned _sp = 0; while (cond) { __builtin_amdgcn_s_sleep(1); \
;     if ((++_sp & 255u) == 0u) { if (xb_ld(&(bar)[XB_TMO])) break; if (_sp > XB_SPIN_CAP) { atomicAdd(&(bar)[XB_TMO], 1u); break; } } } } while (0)
; __device__ __forceinline__ void xcd_barrier(const XcdBarrier& b) {
;     ...
;         if (old + 1u == (gen + 1u) * nloc) {
;             __builtin_amdgcn_fence(__ATOMIC_RELEASE, "agent");
;             asm volatile("s_waitcnt vmcnt(0)" ::: "memory");
;             const unsigned og = xb_add(&bar[XB_TOP], 1u);
;             const unsigned tg = og / nx;
;             if (og + 1u == (tg + 1u) * nx) xb_add(&bar[XB_TOPGEN], 1u);
;             else XB_SPIN(xb_ld(&bar[XB_TOPGEN]) == tg, bar);
;             __builtin_amdgcn_fence(__ATOMIC_ACQUIRE, "agent");
;             xb_add(&bar[XB_XGEN(b.x)], 1u);
;             asm volatile("s_waitcnt vmcnt(0)" ::: "memory");
.LBB0_860:
	s_or_b64 exec, exec, s[6:7]
.LBB0_861:
	s_or_b64 exec, exec, s[0:1]
	s_waitcnt lgkmcnt(0)
	s_barrier

; __device__ __forceinline__ unsigned xb_ld(unsigned* p)              { return __hip_atomic_load(p, __ATOMIC_RELAXED, __HIP_MEMORY_SCOPE_AGENT); }
; __device__ __forceinline__ unsigned xb_add(unsigned* p, unsigned v) { return __hip_atomic_fetch_add(p, v, __ATOMIC_RELAXED, __HIP_MEMORY_SCOPE_AGENT); }
; #define XB_SPIN(cond, bar) do { unsigned _sp = 0; while (cond) { __builtin_amdgcn_s_sleep(1); \
;     if ((++_sp & 255u) == 0u) { if (xb_ld(&(bar)[XB_TMO])) break; if (_sp > XB_SPIN_CAP) { atomicAdd(&(bar)[XB_TMO], 1u); break; } } } } while (0)
; __device__ __forceinline__ void xcd_barrier(const XcdBarrier& b) {
;     ...
;         if (old + 1u == (gen + 1u) * nloc) {
;             __builtin_amdgcn_fence(__ATOMIC_RELEASE, "agent");
;             asm volatile("s_waitcnt vmcnt(0)" ::: "memory");
;             const unsigned og = xb_add(&bar[XB_TOP], 1u);
;             const unsigned tg = og / nx;
;             if (og + 1u == (tg + 1u) * nx) xb_add(&bar[XB_TOPGEN], 1u);
;             else XB_SPIN(xb_ld(&bar[XB_TOPGEN]) == tg, bar);
;             __builtin_amdgcn_fence(__ATOMIC_ACQUIRE, "agent");
;             xb_add(&bar[XB_XGEN(b.x)], 1u);
;             asm volatile("s_waitcnt vmcnt(0)" ::: "memory");
.LBB0_927:
	s_or_b64 exec, exec, s[6:7]
.LBB0_928:
	s_or_b64 exec, exec, s[0:1]
	s_waitcnt lgkmcnt(0)
	s_barrier

; __device__ __forceinline__ unsigned xb_ld(unsigned* p)              { return __hip_atomic_load(p, __ATOMIC_RELAXED, __HIP_MEMORY_SCOPE_AGENT); }
; __device__ __forceinline__ unsigned xb_add(unsigned* p, unsigned v) { return __hip_atomic_fetch_add(p, v, __ATOMIC_RELAXED, __HIP_MEMORY_SCOPE_AGENT); }
; #define XB_SPIN(cond, bar) do { unsigned _sp = 0; while (cond) { __builtin_amdgcn_s_sleep(1); \
;     if ((++_sp & 255u) == 0u) { if (xb_ld(&(bar)[XB_TMO])) break; if (_sp > XB_SPIN_CAP) { atomicAdd(&(bar)[XB_TMO], 1u); break; } } } } while (0)
; __device__ __forceinline__ void xcd_barrier(const XcdBarrier& b) {
;     ...
;         if (old + 1u == (gen + 1u) * nloc) {
;             __builtin_amdgcn_fence(__ATOMIC_RELEASE, "agent");
;             asm volatile("s_waitcnt vmcnt(0)" ::: "memory");
;             const unsigned og = xb_add(&bar[XB_TOP], 1u);
;             const unsigned tg = og / nx;
;             if (og + 1u == (tg + 1u) * nx) xb_add(&bar[XB_TOPGEN], 1u);
;             else XB_SPIN(xb_ld(&bar[XB_TOPGEN]) == tg, bar);
;             __builtin_amdgcn_fence(__ATOMIC_ACQUIRE, "agent");
;             xb_add(&bar[XB_XGEN(b.x)], 1u);
;             asm volatile("s_waitcnt vmcnt(0)" ::: "memory");
.LBB0_1006:
	s_or_b64 exec, exec, s[6:7]
.LBB0_1007:
	s_or_b64 exec, exec, s[0:1]
	s_waitcnt lgkmcnt(0)
	s_barrier

; __device__ __forceinline__ unsigned xb_ld(unsigned* p)              { return __hip_atomic_load(p, __ATOMIC_RELAXED, __HIP_MEMORY_SCOPE_AGENT); }
; __device__ __forceinline__ unsigned xb_add(unsigned* p, unsigned v) { return __hip_atomic_fetch_add(p, v, __ATOMIC_RELAXED, __HIP_MEMORY_SCOPE_AGENT); }
; #define XB_SPIN(cond, bar) do { unsigned _sp = 0; while (cond) { __builtin_amdgcn_s_sleep(1); \
;     if ((++_sp & 255u) == 0u) { if (xb_ld(&(bar)[XB_TMO])) break; if (_sp > XB_SPIN_CAP) { atomicAdd(&(bar)[XB_TMO], 1u); break; } } } } while (0)
; __device__ __forceinline__ void xcd_barrier(const XcdBarrier& b) {
;     ...
;         if (old + 1u == (gen + 1u) * nloc) {
;             __builtin_amdgcn_fence(__ATOMIC_RELEASE, "agent");
;             asm volatile("s_waitcnt vmcnt(0)" ::: "memory");
;             const unsigned og = xb_add(&bar[XB_TOP], 1u);
;             const unsigned tg = og / nx;
;             if (og + 1u == (tg + 1u) * nx) xb_add(&bar[XB_TOPGEN], 1u);
;             else XB_SPIN(xb_ld(&bar[XB_TOPGEN]) == tg, bar);
;             __builtin_amdgcn_fence(__ATOMIC_ACQUIRE, "agent");
;             xb_add(&bar[XB_XGEN(b.x)], 1u);
;             asm volatile("s_waitcnt vmcnt(0)" ::: "memory");
.LBB0_1064:
	s_or_b64 exec, exec, s[6:7]
.LBB0_1065:
	s_or_b64 exec, exec, s[0:1]
	s_waitcnt lgkmcnt(0)
	s_barrier

; __device__ __forceinline__ unsigned xb_ld(unsigned* p)              { return __hip_atomic_load(p, __ATOMIC_RELAXED, __HIP_MEMORY_SCOPE_AGENT); }
; __device__ __forceinline__ unsigned xb_add(unsigned* p, unsigned v) { return __hip_atomic_fetch_add(p, v, __ATOMIC_RELAXED, __HIP_MEMORY_SCOPE_AGENT); }
; #define XB_SPIN(cond, bar) do { unsigned _sp = 0; while (cond) { __builtin_amdgcn_s_sleep(1); \
;     if ((++_sp & 255u) == 0u) { if (xb_ld(&(bar)[XB_TMO])) break; if (_sp > XB_SPIN_CAP) { atomicAdd(&(bar)[XB_TMO], 1u); break; } } } } while (0)
; __device__ __forceinline__ void xcd_barrier(const XcdBarrier& b) {
;     ...
;         if (old + 1u == (gen + 1u) * nloc) {
;             __builtin_amdgcn_fence(__ATOMIC_RELEASE, "agent");
;             asm volatile("s_waitcnt vmcnt(0)" ::: "memory");
;             const unsigned og = xb_add(&bar[XB_TOP], 1u);
;             const unsigned tg = og / nx;
;             if (og + 1u == (tg + 1u) * nx) xb_add(&bar[XB_TOPGEN], 1u);
;             else XB_SPIN(xb_ld(&bar[XB_TOPGEN]) == tg, bar);
;             __builtin_amdgcn_fence(__ATOMIC_ACQUIRE, "agent");
;             xb_add(&bar[XB_XGEN(b.x)], 1u);
;             asm volatile("s_waitcnt vmcnt(0)" ::: "memory");
.LBB0_1163:
	s_or_b64 exec, exec, s[6:7]
.LBB0_1164:
	s_or_b64 exec, exec, s[0:1]
	s_waitcnt lgkmcnt(0)
	s_barrier

; __device__ __forceinline__ unsigned xb_ld(unsigned* p)              { return __hip_atomic_load(p, __ATOMIC_RELAXED, __HIP_MEMORY_SCOPE_AGENT); }
; __device__ __forceinline__ unsigned xb_add(unsigned* p, unsigned v) { return __hip_atomic_fetch_add(p, v, __ATOMIC_RELAXED, __HIP_MEMORY_SCOPE_AGENT); }
; #define XB_SPIN(cond, bar) do { unsigned _sp = 0; while (cond) { __builtin_amdgcn_s_sleep(1); \
;     if ((++_sp & 255u) == 0u) { if (xb_ld(&(bar)[XB_TMO])) break; if (_sp > XB_SPIN_CAP) { atomicAdd(&(bar)[XB_TMO], 1u); break; } } } } while (0)
; __device__ __forceinline__ void xcd_barrier(const XcdBarrier& b) {
;     ...
;         if (old + 1u == (gen + 1u) * nloc) {
;             __builtin_amdgcn_fence(__ATOMIC_RELEASE, "agent");
;             asm volatile("s_waitcnt vmcnt(0)" ::: "memory");
;             const unsigned og = xb_add(&bar[XB_TOP], 1u);
;             const unsigned tg = og / nx;
;             if (og + 1u == (tg + 1u) * nx) xb_add(&bar[XB_TOPGEN], 1u);
;             else XB_SPIN(xb_ld(&bar[XB_TOPGEN]) == tg, bar);
;             __builtin_amdgcn_fence(__ATOMIC_ACQUIRE, "agent");
;             xb_add(&bar[XB_XGEN(b.x)], 1u);
;             asm volatile("s_waitcnt vmcnt(0)" ::: "memory");
.LBB0_1283:
	s_or_b64 exec, exec, s[6:7]
.LBB0_1284:
	s_or_b64 exec, exec, s[2:3]
	s_waitcnt lgkmcnt(0)
	s_barrier

; __device__ __forceinline__ unsigned xb_ld(unsigned* p)              { return __hip_atomic_load(p, __ATOMIC_RELAXED, __HIP_MEMORY_SCOPE_AGENT); }
; __device__ __forceinline__ unsigned xb_add(unsigned* p, unsigned v) { return __hip_atomic_fetch_add(p, v, __ATOMIC_RELAXED, __HIP_MEMORY_SCOPE_AGENT); }
; #define XB_SPIN(cond, bar) do { unsigned _sp = 0; while (cond) { __builtin_amdgcn_s_sleep(1); \
;     if ((++_sp & 255u) == 0u) { if (xb_ld(&(bar)[XB_TMO])) break; if (_sp > XB_SPIN_CAP) { atomicAdd(&(bar)[XB_TMO], 1u); break; } } } } while (0)
; __device__ __forceinline__ void xcd_barrier(const XcdBarrier& b) {
;     ...
;         if (old + 1u == (gen + 1u) * nloc) {
;             __builtin_amdgcn_fence(__ATOMIC_RELEASE, "agent");
;             asm volatile("s_waitcnt vmcnt(0)" ::: "memory");
;             const unsigned og = xb_add(&bar[XB_TOP], 1u);
;             const unsigned tg = og / nx;
;             if (og + 1u == (tg + 1u) * nx) xb_add(&bar[XB_TOPGEN], 1u);
;             else XB_SPIN(xb_ld(&bar[XB_TOPGEN]) == tg, bar);
;             __builtin_amdgcn_fence(__ATOMIC_ACQUIRE, "agent");
;             xb_add(&bar[XB_XGEN(b.x)], 1u);
;             asm volatile("s_waitcnt vmcnt(0)" ::: "memory");
.LBB0_1436:
	s_or_b64 exec, exec, s[6:7]
.LBB0_1437:
	s_or_b64 exec, exec, s[2:3]
	s_waitcnt lgkmcnt(0)
	s_barrier

; __device__ __forceinline__ unsigned xb_ld(unsigned* p)              { return __hip_atomic_load(p, __ATOMIC_RELAXED, __HIP_MEMORY_SCOPE_AGENT); }
; __device__ __forceinline__ unsigned xb_add(unsigned* p, unsigned v) { return __hip_atomic_fetch_add(p, v, __ATOMIC_RELAXED, __HIP_MEMORY_SCOPE_AGENT); }
; #define XB_SPIN(cond, bar) do { unsigned _sp = 0; while (cond) { __builtin_amdgcn_s_sleep(1); \
;     if ((++_sp & 255u) == 0u) { if (xb_ld(&(bar)[XB_TMO])) break; if (_sp > XB_SPIN_CAP) { atomicAdd(&(bar)[XB_TMO], 1u); break; } } } } while (0)
; __device__ __forceinline__ void xcd_barrier(const XcdBarrier& b) {
;     ...
;         if (old + 1u == (gen + 1u) * nloc) {
;             __builtin_amdgcn_fence(__ATOMIC_RELEASE, "agent");
;             asm volatile("s_waitcnt vmcnt(0)" ::: "memory");
;             const unsigned og = xb_add(&bar[XB_TOP], 1u);
;             const unsigned tg = og / nx;
;             if (og + 1u == (tg + 1u) * nx) xb_add(&bar[XB_TOPGEN], 1u);
;             else XB_SPIN(xb_ld(&bar[XB_TOPGEN]) == tg, bar);
;             __builtin_amdgcn_fence(__ATOMIC_ACQUIRE, "agent");
;             xb_add(&bar[XB_XGEN(b.x)], 1u);
;             asm volatile("s_waitcnt vmcnt(0)" ::: "memory");
.LBB0_1511:
	s_or_b64 exec, exec, s[6:7]
.LBB0_1512:
	s_or_b64 exec, exec, s[0:1]
	s_waitcnt lgkmcnt(0)
	s_barrier

; __device__ __forceinline__ unsigned xb_ld(unsigned* p)              { return __hip_atomic_load(p, __ATOMIC_RELAXED, __HIP_MEMORY_SCOPE_AGENT); }
; __device__ __forceinline__ unsigned xb_add(unsigned* p, unsigned v) { return __hip_atomic_fetch_add(p, v, __ATOMIC_RELAXED, __HIP_MEMORY_SCOPE_AGENT); }
; #define XB_SPIN(cond, bar) do { unsigned _sp = 0; while (cond) { __builtin_amdgcn_s_sleep(1); \
;     if ((++_sp & 255u) == 0u) { if (xb_ld(&(bar)[XB_TMO])) break; if (_sp > XB_SPIN_CAP) { atomicAdd(&(bar)[XB_TMO], 1u); break; } } } } while (0)
; __device__ __forceinline__ void xcd_barrier(const XcdBarrier& b) {
;     ...
;         if (old + 1u == (gen + 1u) * nloc) {
;             __builtin_amdgcn_fence(__ATOMIC_RELEASE, "agent");
;             asm volatile("s_waitcnt vmcnt(0)" ::: "memory");
;             const unsigned og = xb_add(&bar[XB_TOP], 1u);
;             const unsigned tg = og / nx;
;             if (og + 1u == (tg + 1u) * nx) xb_add(&bar[XB_TOPGEN], 1u);
;             else XB_SPIN(xb_ld(&bar[XB_TOPGEN]) == tg, bar);
;             __builtin_amdgcn_fence(__ATOMIC_ACQUIRE, "agent");
;             xb_add(&bar[XB_XGEN(b.x)], 1u);
;             asm volatile("s_waitcnt vmcnt(0)" ::: "memory");
.LBB0_1593:
	s_or_b64 exec, exec, s[6:7]
.LBB0_1594:
	s_or_b64 exec, exec, s[2:3]
	s_waitcnt lgkmcnt(0)
	s_barrier

; __device__ __forceinline__ unsigned xb_ld(unsigned* p)              { return __hip_atomic_load(p, __ATOMIC_RELAXED, __HIP_MEMORY_SCOPE_AGENT); }
; __device__ __forceinline__ unsigned xb_add(unsigned* p, unsigned v) { return __hip_atomic_fetch_add(p, v, __ATOMIC_RELAXED, __HIP_MEMORY_SCOPE_AGENT); }
; #define XB_SPIN(cond, bar) do { unsigned _sp = 0; while (cond) { __builtin_amdgcn_s_sleep(1); \
;     if ((++_sp & 255u) == 0u) { if (xb_ld(&(bar)[XB_TMO])) break; if (_sp > XB_SPIN_CAP) { atomicAdd(&(bar)[XB_TMO], 1u); break; } } } } while (0)
; __device__ __forceinline__ void xcd_barrier(const XcdBarrier& b) {
;     ...
;     if (threadIdx.x == 0) {
;         unsigned* bar = b.bar;
;         __builtin_amdgcn_s_waitcnt(0);
;         unsigned nloc = b.st[0], nx = b.st[1];
;         if (nloc == 0u) { xcd_barrier_complete(bar, b.x, nloc, nx); b.st[0] = nloc; b.st[1] = nx; }
;         const unsigned old = xb_add(&bar[XB_XSUB(b.x)], 1u);
;         const unsigned gen = old / nloc;
;         if (old + 1u == (gen + 1u) * nloc) {
;             __builtin_amdgcn_fence(__ATOMIC_RELEASE, "agent");
;             asm volatile("s_waitcnt vmcnt(0)" ::: "memory");
;             const unsigned og = xb_add(&bar[XB_TOP], 1u);
;             const unsigned tg = og / nx;
;             if (og + 1u == (tg + 1u) * nx) xb_add(&bar[XB_TOPGEN], 1u);
;             else XB_SPIN(xb_ld(&bar[XB_TOPGEN]) == tg, bar);
;             __builtin_amdgcn_fence(__ATOMIC_ACQUIRE, "agent");
;             xb_add(&bar[XB_XGEN(b.x)], 1u);
;             asm volatile("s_waitcnt vmcnt(0)" ::: "memory");
;         } else {
;             XB_SPIN(xb_ld(&bar[XB_XGEN(b.x)]) == gen, bar);
.LBB0_1742:
	v_readlane_b32 s4, v247, 7
	s_lshl_b32 s4, s4, 8
	s_add_u32 s4, s72, s4
	s_addc_u32 s5, s73, 0
	v_mov_b32_e32 v2, 0x1000
	v_mov_b32_e32 v4, 1
	global_atomic_add v4, v2, v4, s[4:5] offset:1024 sc0
	buffer_inv sc1
	v_cvt_f32_u32_e32 v2, v3
	v_sub_u32_e32 v5, 0, v3
	v_rcp_iflag_f32_e32 v2, v2
	s_nop 0
	v_mul_f32_e32 v2, 0x4f7ffffe, v2
	v_cvt_u32_f32_e32 v2, v2
	v_mul_lo_u32 v5, v5, v2
	v_mul_hi_u32 v5, v2, v5
	v_add_u32_e32 v2, v2, v5
	s_waitcnt vmcnt(1)
	v_mul_hi_u32 v2, v4, v2
	v_mul_lo_u32 v5, v2, v3
	v_sub_u32_e32 v5, v4, v5
	v_add_u32_e32 v6, 1, v2
	v_cmp_ge_u32_e32 vcc, v5, v3
	v_add_u32_e32 v4, 1, v4
	s_nop 0
	v_cndmask_b32_e32 v2, v2, v6, vcc
	v_sub_u32_e32 v6, v5, v3
	v_cndmask_b32_e32 v5, v5, v6, vcc
	v_add_u32_e32 v6, 1, v2
	v_cmp_ge_u32_e32 vcc, v5, v3
	s_nop 1
	v_cndmask_b32_e32 v2, v2, v6, vcc
	v_mul_lo_u32 v5, v3, v2
	v_add_u32_e32 v3, v5, v3
	v_cmp_ne_u32_e32 vcc, v4, v3
	s_and_saveexec_b64 s[6:7], vcc
	s_xor_b64 s[6:7], exec, s[6:7]
	s_cbranch_execz .LBB0_1756
	s_waitcnt lgkmcnt(0)
	v_mov_b32_e32 v1, 0x7100
	global_load_dword v1, v1, s[86:87] offset:1024 sc1
	s_add_u32 s14, s86, 0x7500
	s_addc_u32 s15, s87, 0
	s_waitcnt vmcnt(0)
	v_cmp_eq_u32_e32 vcc, v1, v2
	s_and_saveexec_b64 s[10:11], vcc
	s_cbranch_execz .LBB0_1755
	s_add_u32 s12, s86, 0x4200
	s_addc_u32 s13, s87, 0
	s_mov_b32 s26, 1
	s_mov_b64 s[16:17], 0
	v_mov_b32_e32 v1, 0
	s_branch .LBB0_1746

; __device__ __forceinline__ unsigned xb_ld(unsigned* p)              { return __hip_atomic_load(p, __ATOMIC_RELAXED, __HIP_MEMORY_SCOPE_AGENT); }
; __device__ __forceinline__ unsigned xb_add(unsigned* p, unsigned v) { return __hip_atomic_fetch_add(p, v, __ATOMIC_RELAXED, __HIP_MEMORY_SCOPE_AGENT); }
; #define XB_SPIN(cond, bar) do { unsigned _sp = 0; while (cond) { __builtin_amdgcn_s_sleep(1); \
;     if ((++_sp & 255u) == 0u) { if (xb_ld(&(bar)[XB_TMO])) break; if (_sp > XB_SPIN_CAP) { atomicAdd(&(bar)[XB_TMO], 1u); break; } } } } while (0)
; __device__ __forceinline__ void xcd_barrier(const XcdBarrier& b) {
;     ...
;         if (old + 1u == (gen + 1u) * nloc) {
;             __builtin_amdgcn_fence(__ATOMIC_RELEASE, "agent");
;             asm volatile("s_waitcnt vmcnt(0)" ::: "memory");
;             const unsigned og = xb_add(&bar[XB_TOP], 1u);
;             const unsigned tg = og / nx;
;             if (og + 1u == (tg + 1u) * nx) xb_add(&bar[XB_TOPGEN], 1u);
;             else XB_SPIN(xb_ld(&bar[XB_TOPGEN]) == tg, bar);
;             __builtin_amdgcn_fence(__ATOMIC_ACQUIRE, "agent");
;             xb_add(&bar[XB_XGEN(b.x)], 1u);
;             asm volatile("s_waitcnt vmcnt(0)" ::: "memory");
.LBB0_1773:
	s_or_b64 exec, exec, s[6:7]
.LBB0_1774:
	s_or_b64 exec, exec, s[2:3]
	s_waitcnt lgkmcnt(0)
	s_barrier

; __device__ __forceinline__ unsigned xb_ld(unsigned* p)              { return __hip_atomic_load(p, __ATOMIC_RELAXED, __HIP_MEMORY_SCOPE_AGENT); }
; __device__ __forceinline__ unsigned xb_add(unsigned* p, unsigned v) { return __hip_atomic_fetch_add(p, v, __ATOMIC_RELAXED, __HIP_MEMORY_SCOPE_AGENT); }
; #define XB_SPIN(cond, bar) do { unsigned _sp = 0; while (cond) { __builtin_amdgcn_s_sleep(1); \
;     if ((++_sp & 255u) == 0u) { if (xb_ld(&(bar)[XB_TMO])) break; if (_sp > XB_SPIN_CAP) { atomicAdd(&(bar)[XB_TMO], 1u); break; } } } } while (0)
; __device__ __forceinline__ void xcd_barrier(const XcdBarrier& b) {
;     ...
;         if (old + 1u == (gen + 1u) * nloc) {
;             __builtin_amdgcn_fence(__ATOMIC_RELEASE, "agent");
;             asm volatile("s_waitcnt vmcnt(0)" ::: "memory");
;             const unsigned og = xb_add(&bar[XB_TOP], 1u);
;             const unsigned tg = og / nx;
;             if (og + 1u == (tg + 1u) * nx) xb_add(&bar[XB_TOPGEN], 1u);
;             else XB_SPIN(xb_ld(&bar[XB_TOPGEN]) == tg, bar);
;             __builtin_amdgcn_fence(__ATOMIC_ACQUIRE, "agent");
;             xb_add(&bar[XB_XGEN(b.x)], 1u);
;             asm volatile("s_waitcnt vmcnt(0)" ::: "memory");
.LBB0_1938:
	s_or_b64 exec, exec, s[6:7]
.LBB0_1939:
	s_or_b64 exec, exec, s[2:3]
	s_waitcnt lgkmcnt(0)
	s_barrier

; __device__ __forceinline__ unsigned xb_ld(unsigned* p)              { return __hip_atomic_load(p, __ATOMIC_RELAXED, __HIP_MEMORY_SCOPE_AGENT); }
; __device__ __forceinline__ unsigned xb_add(unsigned* p, unsigned v) { return __hip_atomic_fetch_add(p, v, __ATOMIC_RELAXED, __HIP_MEMORY_SCOPE_AGENT); }
; #define XB_SPIN(cond, bar) do { unsigned _sp = 0; while (cond) { __builtin_amdgcn_s_sleep(1); \
;     if ((++_sp & 255u) == 0u) { if (xb_ld(&(bar)[XB_TMO])) break; if (_sp > XB_SPIN_CAP) { atomicAdd(&(bar)[XB_TMO], 1u); break; } } } } while (0)
; __device__ __forceinline__ void xcd_barrier(const XcdBarrier& b) {
;     ...
;     if (threadIdx.x == 0) {
;         unsigned* bar = b.bar;
;         __builtin_amdgcn_s_waitcnt(0);
;         unsigned nloc = b.st[0], nx = b.st[1];
;         if (nloc == 0u) { xcd_barrier_complete(bar, b.x, nloc, nx); b.st[0] = nloc; b.st[1] = nx; }
;         const unsigned old = xb_add(&bar[XB_XSUB(b.x)], 1u);
;         const unsigned gen = old / nloc;
;         if (old + 1u == (gen + 1u) * nloc) {
;             __builtin_amdgcn_fence(__ATOMIC_RELEASE, "agent");
;             asm volatile("s_waitcnt vmcnt(0)" ::: "memory");
;             const unsigned og = xb_add(&bar[XB_TOP], 1u);
;             const unsigned tg = og / nx;
;             if (og + 1u == (tg + 1u) * nx) xb_add(&bar[XB_TOPGEN], 1u);
;             else XB_SPIN(xb_ld(&bar[XB_TOPGEN]) == tg, bar);
;             __builtin_amdgcn_fence(__ATOMIC_ACQUIRE, "agent");
;             xb_add(&bar[XB_XGEN(b.x)], 1u);
;             asm volatile("s_waitcnt vmcnt(0)" ::: "memory");
;         } else {
;             XB_SPIN(xb_ld(&bar[XB_XGEN(b.x)]) == gen, bar);
.LBB0_2077:
	v_readlane_b32 s0, v247, 7
	s_lshl_b32 s0, s0, 8
	s_add_u32 s0, s72, s0
	s_addc_u32 s1, s73, 0
	v_mov_b32_e32 v3, 0x1000
	v_mov_b32_e32 v5, 1
	global_atomic_add v5, v3, v5, s[0:1] offset:1024 sc0
	buffer_inv sc1
	v_cvt_f32_u32_e32 v3, v4
	v_sub_u32_e32 v6, 0, v4
	v_rcp_iflag_f32_e32 v3, v3
	s_nop 0
	v_mul_f32_e32 v3, 0x4f7ffffe, v3
	v_cvt_u32_f32_e32 v3, v3
	v_mul_lo_u32 v6, v6, v3
	v_mul_hi_u32 v6, v3, v6
	v_add_u32_e32 v3, v3, v6
	s_waitcnt vmcnt(1)
	v_mul_hi_u32 v3, v5, v3
	v_mul_lo_u32 v6, v3, v4
	v_sub_u32_e32 v6, v5, v6
	v_add_u32_e32 v7, 1, v3
	v_cmp_ge_u32_e32 vcc, v6, v4
	v_add_u32_e32 v5, 1, v5
	s_nop 0
	v_cndmask_b32_e32 v3, v3, v7, vcc
	v_sub_u32_e32 v7, v6, v4
	v_cndmask_b32_e32 v6, v6, v7, vcc
	v_add_u32_e32 v7, 1, v3
	v_cmp_ge_u32_e32 vcc, v6, v4
	s_nop 1
	v_cndmask_b32_e32 v3, v3, v7, vcc
	v_mul_lo_u32 v6, v4, v3
	v_add_u32_e32 v4, v6, v4
	v_cmp_ne_u32_e32 vcc, v5, v4
	s_and_saveexec_b64 s[4:5], vcc
	s_xor_b64 s[4:5], exec, s[4:5]
	s_cbranch_execz .LBB0_2091
	s_waitcnt lgkmcnt(0)
	v_mov_b32_e32 v2, 0x7100
	global_load_dword v2, v2, s[86:87] offset:1024 sc1
	s_add_u32 s14, s86, 0x7500
	s_addc_u32 s15, s87, 0
	s_waitcnt vmcnt(0)
	v_cmp_eq_u32_e32 vcc, v2, v3
	s_and_saveexec_b64 s[6:7], vcc
	s_cbranch_execz .LBB0_2090
	s_add_u32 s12, s86, 0x4200
	s_addc_u32 s13, s87, 0
	s_mov_b32 s26, 1
	s_mov_b64 s[16:17], 0
	v_mov_b32_e32 v2, 0
	s_branch .LBB0_2081

; #define LAS __attribute__((address_space(3)))
; __device__ __forceinline__ unsigned xb_ld(unsigned* p)              { return __hip_atomic_load(p, __ATOMIC_RELAXED, __HIP_MEMORY_SCOPE_AGENT); }
; __device__ __forceinline__ unsigned xb_add(unsigned* p, unsigned v) { return __hip_atomic_fetch_add(p, v, __ATOMIC_RELAXED, __HIP_MEMORY_SCOPE_AGENT); }
; #define XB_SPIN(cond, bar) do { unsigned _sp = 0; while (cond) { __builtin_amdgcn_s_sleep(1); \
;     if ((++_sp & 255u) == 0u) { if (xb_ld(&(bar)[XB_TMO])) break; if (_sp > XB_SPIN_CAP) { atomicAdd(&(bar)[XB_TMO], 1u); break; } } } } while (0)
; __device__ __forceinline__ void xcd_barrier(const XcdBarrier& b) {
;     ...
;         if (old + 1u == (gen + 1u) * nloc) {
;             __builtin_amdgcn_fence(__ATOMIC_RELEASE, "agent");
;             asm volatile("s_waitcnt vmcnt(0)" ::: "memory");
;             const unsigned og = xb_add(&bar[XB_TOP], 1u);
;             const unsigned tg = og / nx;
;             if (og + 1u == (tg + 1u) * nx) xb_add(&bar[XB_TOPGEN], 1u);
;             else XB_SPIN(xb_ld(&bar[XB_TOPGEN]) == tg, bar);
;             __builtin_amdgcn_fence(__ATOMIC_ACQUIRE, "agent");
;             xb_add(&bar[XB_XGEN(b.x)], 1u);
;             asm volatile("s_waitcnt vmcnt(0)" ::: "memory");
; __global__ void __launch_bounds__(NWAVES * 64, 2) hybrid_fwd(Args args) {
;     ...
;         LAS int* late = (LAS int*)(F.lds + MISC_OFF + 4096);
;         for (int i = F.tid; i < 192; i += NWAVES * 64) late[i] = (i >= Tf && i < T) ? 1 : 0;
;         __syncthreads();
.LBB0_2108:
	s_or_b64 exec, exec, s[4:5]
.LBB0_2109:
	s_or_b64 exec, exec, s[2:3]
	s_movk_i32 s0, 0xc0
	v_cmp_gt_u32_e32 vcc, s0, v0
	s_waitcnt lgkmcnt(0)
	s_barrier
	s_and_saveexec_b64 s[2:3], vcc
	s_cbranch_execz .LBB0_2111
	v_cmp_le_i32_e32 vcc, s48, v0
	v_cmp_gt_i32_e64 s[0:1], s33, v0
	s_and_b64 s[0:1], vcc, s[0:1]
	v_add_u32_e32 v3, 0x21000, v187
	v_cndmask_b32_e64 v2, 0, 1, s[0:1]
	ds_write_b32 v3, v2

; __device__ __forceinline__ unsigned xb_ld(unsigned* p)              { return __hip_atomic_load(p, __ATOMIC_RELAXED, __HIP_MEMORY_SCOPE_AGENT); }
; __device__ __forceinline__ unsigned xb_add(unsigned* p, unsigned v) { return __hip_atomic_fetch_add(p, v, __ATOMIC_RELAXED, __HIP_MEMORY_SCOPE_AGENT); }
; #define XB_SPIN(cond, bar) do { unsigned _sp = 0; while (cond) { __builtin_amdgcn_s_sleep(1); \
;     if ((++_sp & 255u) == 0u) { if (xb_ld(&(bar)[XB_TMO])) break; if (_sp > XB_SPIN_CAP) { atomicAdd(&(bar)[XB_TMO], 1u); break; } } } } while (0)
; __device__ __forceinline__ void xcd_barrier(const XcdBarrier& b) {
;     ...
;     if (threadIdx.x == 0) {
;         unsigned* bar = b.bar;
;         __builtin_amdgcn_s_waitcnt(0);
;         unsigned nloc = b.st[0], nx = b.st[1];
;         if (nloc == 0u) { xcd_barrier_complete(bar, b.x, nloc, nx); b.st[0] = nloc; b.st[1] = nx; }
;         const unsigned old = xb_add(&bar[XB_XSUB(b.x)], 1u);
;         const unsigned gen = old / nloc;
;         if (old + 1u == (gen + 1u) * nloc) {
;             __builtin_amdgcn_fence(__ATOMIC_RELEASE, "agent");
;             asm volatile("s_waitcnt vmcnt(0)" ::: "memory");
;             const unsigned og = xb_add(&bar[XB_TOP], 1u);
;             const unsigned tg = og / nx;
;             if (og + 1u == (tg + 1u) * nx) xb_add(&bar[XB_TOPGEN], 1u);
;             else XB_SPIN(xb_ld(&bar[XB_TOPGEN]) == tg, bar);
;             __builtin_amdgcn_fence(__ATOMIC_ACQUIRE, "agent");
;             xb_add(&bar[XB_XGEN(b.x)], 1u);
;             asm volatile("s_waitcnt vmcnt(0)" ::: "memory");
;         } else {
;             XB_SPIN(xb_ld(&bar[XB_XGEN(b.x)]) == gen, bar);
.LBB0_2157:
	v_readlane_b32 s4, v247, 7
	s_lshl_b32 s4, s4, 8
	s_add_u32 s4, s72, s4
	s_addc_u32 s5, s73, 0
	v_mov_b32_e32 v1, 0x1000
	v_mov_b32_e32 v3, 1
	global_atomic_add v3, v1, v3, s[4:5] offset:1024 sc0
	buffer_inv sc1
	v_cvt_f32_u32_e32 v1, v2
	v_sub_u32_e32 v4, 0, v2
	v_rcp_iflag_f32_e32 v1, v1
	s_nop 0
	v_mul_f32_e32 v1, 0x4f7ffffe, v1
	v_cvt_u32_f32_e32 v1, v1
	v_mul_lo_u32 v4, v4, v1
	v_mul_hi_u32 v4, v1, v4
	v_add_u32_e32 v1, v1, v4
	s_waitcnt vmcnt(1)
	v_mul_hi_u32 v1, v3, v1
	v_mul_lo_u32 v4, v1, v2
	v_sub_u32_e32 v4, v3, v4
	v_add_u32_e32 v5, 1, v1
	v_cmp_ge_u32_e32 vcc, v4, v2
	v_add_u32_e32 v3, 1, v3
	s_nop 0
	v_cndmask_b32_e32 v1, v1, v5, vcc
	v_sub_u32_e32 v5, v4, v2
	v_cndmask_b32_e32 v4, v4, v5, vcc
	v_add_u32_e32 v5, 1, v1
	v_cmp_ge_u32_e32 vcc, v4, v2
	s_nop 1
	v_cndmask_b32_e32 v1, v1, v5, vcc
	v_mul_lo_u32 v4, v2, v1
	v_add_u32_e32 v2, v4, v2
	v_cmp_ne_u32_e32 vcc, v3, v2
	s_and_saveexec_b64 s[6:7], vcc
	s_xor_b64 s[6:7], exec, s[6:7]
	s_cbranch_execz .LBB0_2171
	s_waitcnt lgkmcnt(0)
	v_mov_b32_e32 v0, 0x7100
	global_load_dword v0, v0, s[86:87] offset:1024 sc1
	s_add_u32 s14, s86, 0x7500
	s_addc_u32 s15, s87, 0
	s_waitcnt vmcnt(0)
	v_cmp_eq_u32_e32 vcc, v0, v1
	s_and_saveexec_b64 s[10:11], vcc
	s_cbranch_execz .LBB0_2170
	s_add_u32 s12, s86, 0x4200
	s_addc_u32 s13, s87, 0
	s_mov_b32 s26, 1
	s_mov_b64 s[16:17], 0
	v_mov_b32_e32 v0, 0
	s_branch .LBB0_2161

; __device__ __forceinline__ unsigned xb_ld(unsigned* p)              { return __hip_atomic_load(p, __ATOMIC_RELAXED, __HIP_MEMORY_SCOPE_AGENT); }
; __device__ __forceinline__ unsigned xb_add(unsigned* p, unsigned v) { return __hip_atomic_fetch_add(p, v, __ATOMIC_RELAXED, __HIP_MEMORY_SCOPE_AGENT); }
; #define XB_SPIN(cond, bar) do { unsigned _sp = 0; while (cond) { __builtin_amdgcn_s_sleep(1); \
;     if ((++_sp & 255u) == 0u) { if (xb_ld(&(bar)[XB_TMO])) break; if (_sp > XB_SPIN_CAP) { atomicAdd(&(bar)[XB_TMO], 1u); break; } } } } while (0)
; __device__ __forceinline__ void xcd_barrier(const XcdBarrier& b) {
;     ...
;         if (old + 1u == (gen + 1u) * nloc) {
;             __builtin_amdgcn_fence(__ATOMIC_RELEASE, "agent");
;             asm volatile("s_waitcnt vmcnt(0)" ::: "memory");
;             const unsigned og = xb_add(&bar[XB_TOP], 1u);
;             const unsigned tg = og / nx;
;             if (og + 1u == (tg + 1u) * nx) xb_add(&bar[XB_TOPGEN], 1u);
;             else XB_SPIN(xb_ld(&bar[XB_TOPGEN]) == tg, bar);
;             __builtin_amdgcn_fence(__ATOMIC_ACQUIRE, "agent");
;             xb_add(&bar[XB_XGEN(b.x)], 1u);
;             asm volatile("s_waitcnt vmcnt(0)" ::: "memory");
.LBB0_2188:
	s_or_b64 exec, exec, s[6:7]
.LBB0_2189:
	s_or_b64 exec, exec, s[2:3]
	s_waitcnt lgkmcnt(0)
	s_barrier
